# v8_vinterleave
# speedup vs baseline: 1.0629x; 1.0039x over previous
.LBB1_53:
	ds_read_b128 v[164:167], v205 offset:43008
	ds_read_b128 v[168:171], v205 offset:43040
	ds_read_b128 v[172:175], v205 offset:43072
	ds_read_b128 v[176:179], v205 offset:43104
	ds_read_b128 v[180:183], v205 offset:43136
	ds_read_b128 v[184:187], v205 offset:43168
	ds_read_b128 v[188:191], v205 offset:43200
	ds_read_b128 v[192:195], v205 offset:43232
	s_waitcnt vmcnt(17) lgkmcnt(7)
	v_mfma_f32_32x32x16_f16 v[34:49], v[112:115], v[164:167], 0
	s_waitcnt vmcnt(0)
	v_mfma_f32_32x32x16_f16 v[18:33], v[116:119], v[164:167], v[2:17]
	s_waitcnt lgkmcnt(6)
	v_mfma_f32_32x32x16_f16 v[34:49], v[100:103], v[168:171], v[34:49]
	v_mfma_f32_32x32x16_f16 v[18:33], v[120:123], v[168:171], v[18:33]
	s_waitcnt lgkmcnt(5)
	v_mfma_f32_32x32x16_f16 v[34:49], v[104:107], v[172:175], v[34:49]
	v_mfma_f32_32x32x16_f16 v[18:33], v[124:127], v[172:175], v[18:33]
	s_waitcnt lgkmcnt(4)
	v_mfma_f32_32x32x16_f16 v[34:49], v[108:111], v[176:179], v[34:49]
	v_mfma_f32_32x32x16_f16 v[18:33], v[128:131], v[176:179], v[18:33]
	s_waitcnt lgkmcnt(3)
	v_mfma_f32_32x32x16_f16 v[34:49], v[132:135], v[180:183], v[34:49]
	v_mfma_f32_32x32x16_f16 v[18:33], v[148:151], v[180:183], v[18:33]
	s_waitcnt lgkmcnt(2)
	v_mfma_f32_32x32x16_f16 v[34:49], v[136:139], v[184:187], v[34:49]
	v_mfma_f32_32x32x16_f16 v[18:33], v[152:155], v[184:187], v[18:33]
	s_waitcnt lgkmcnt(1)
	v_mfma_f32_32x32x16_f16 v[34:49], v[140:143], v[188:191], v[34:49]
	v_mfma_f32_32x32x16_f16 v[18:33], v[156:159], v[188:191], v[18:33]
	s_waitcnt lgkmcnt(0)
	v_mfma_f32_32x32x16_f16 v[34:49], v[144:147], v[192:195], v[34:49]
	v_mfma_f32_32x32x16_f16 v[18:33], v[160:163], v[192:195], v[18:33]
	s_nop 10
	v_cvt_pk_f16_f32 v41, v40, v41
	v_cvt_pk_f16_f32 v40, v38, v39
	v_cvt_pk_f16_f32 v39, v36, v37
	v_cvt_pk_f16_f32 v38, v34, v35
	v_cvt_pk_f16_f32 v25, v24, v25
	v_cvt_pk_f16_f32 v24, v22, v23
	v_cvt_pk_f16_f32 v23, v20, v21
	v_cvt_pk_f16_f32 v22, v18, v19
	v_cvt_pk_f16_f32 v21, v48, v49
	v_cvt_pk_f16_f32 v20, v46, v47
	v_cvt_pk_f16_f32 v19, v44, v45
	v_cvt_pk_f16_f32 v18, v42, v43
	v_mfma_f32_32x32x16_f16 v[50:65], v[38:41], v[22:25], 0
	v_cvt_pk_f16_f32 v25, v32, v33
	v_cvt_pk_f16_f32 v24, v30, v31
	v_cvt_pk_f16_f32 v23, v28, v29
	v_cvt_pk_f16_f32 v22, v26, v27
	s_nop 1
	v_mfma_f32_32x32x16_f16 v[34:49], v[18:21], v[22:25], 0
	v_mfma_f32_32x32x16_f16 v[18:33], v[164:167], v[96:99], 0
	v_mfma_f32_32x32x16_f16 v[18:33], v[168:171], v[76:79], v[18:33]
	s_nop 2
	v_max3_f32 v46, v50, v51, v52
	v_max3_f32 v46, v46, v53, v54
	v_max3_f32 v46, v46, v55, v56
	v_max_f32_e32 v47, v61, v61
	v_max_f32_e32 v48, v60, v60
	v_max3_f32 v46, v46, v57, v58
	v_max_f32_e32 v47, v48, v47
	v_mfma_f32_32x32x16_f16 v[18:33], v[172:175], v[72:75], v[18:33]
	v_max3_f32 v47, v46, v59, v47
	v_cndmask_b32_e64 v46, v46, v47, s[0:1]
	v_mov_b32_e32 v47, v46
	s_nop 1
	v_permlane32_swap_b32_e32 v46, v47
	v_max_f32_e32 v47, v47, v47
	v_max_f32_e32 v46, v46, v46
	v_max_f32_e32 v46, v46, v47
	v_mfma_f32_32x32x16_f16 v[18:33], v[176:179], v[68:71], v[18:33]
	v_sub_f32_e32 v47, v50, v46
	v_exp_f32_e32 v50, v47
	v_sub_f32_e32 v47, v51, v46
	v_sub_f32_e32 v48, v52, v46
	v_exp_f32_e32 v51, v47
	v_exp_f32_e32 v52, v48
	v_sub_f32_e32 v48, v53, v46
	v_sub_f32_e32 v49, v55, v46
	v_mfma_f32_32x32x16_f16 v[18:33], v[180:183], v[92:95], v[18:33]
	v_sub_f32_e32 v53, v57, v46
	v_exp_f32_e32 v55, v49
	v_sub_f32_e32 v49, v56, v46
	v_exp_f32_e32 v56, v53
	v_sub_f32_e32 v53, v58, v46
	v_exp_f32_e32 v62, v48
	v_sub_f32_e32 v48, v54, v46
	v_exp_f32_e32 v57, v53
	v_mfma_f32_32x32x16_f16 v[18:33], v[184:187], v[84:87], v[18:33]
	v_sub_f32_e32 v53, v59, v46
	v_add_f32_e32 v47, 0, v50
	v_exp_f32_e32 v48, v48
	v_exp_f32_e32 v53, v53
	v_add_f32_e32 v47, v51, v47
	v_add_f32_e32 v47, v52, v47
	v_exp_f32_e32 v49, v49
	v_add_f32_e32 v47, v62, v47
	v_mfma_f32_32x32x16_f16 v[18:33], v[188:191], v[88:91], v[18:33]
	v_add_f32_e32 v47, v48, v47
	v_cndmask_b32_e64 v58, v53, 0, s[14:15]
	v_sub_f32_e32 v53, v60, v46
	v_sub_f32_e32 v46, v61, v46
	v_add_f32_e32 v47, v55, v47
	v_exp_f32_e32 v53, v53
	v_exp_f32_e32 v46, v46
	v_add_f32_e32 v47, v49, v47
	v_mfma_f32_32x32x16_f16 v[18:33], v[192:195], v[80:83], v[18:33]
	ds_read_b128 v[192:195], v240 offset:48720
	ds_read_b128 v[188:191], v240 offset:48752
	ds_read_b128 v[184:187], v240 offset:48784
	ds_read_b128 v[180:183], v240 offset:48816
	ds_read_b128 v[176:179], v240 offset:48848
	ds_read_b128 v[172:175], v240 offset:48880
	ds_read_b128 v[168:171], v240 offset:48912
	ds_read_b128 v[164:167], v240 offset:48944
	v_add_f32_e32 v47, v56, v47
	v_add_f32_e32 v47, v57, v47
	v_add_f32_e32 v47, v58, v47
	v_cndmask_b32_e64 v59, v53, 0, s[14:15]
	v_cndmask_b32_e64 v60, v46, 0, s[14:15]
	v_cvt_pk_f16_f32 v46, v50, v51
	v_max3_f32 v50, v34, v35, v36
	v_add_f32_e32 v47, v59, v47
	v_max3_f32 v50, v50, v37, v38
	v_add_f32_e32 v53, v60, v47
	v_cvt_pk_f16_f32 v47, v52, v62
	v_max3_f32 v50, v50, v39, v40
	v_max_f32_e32 v51, v45, v45
	v_max_f32_e32 v52, v44, v44
	v_max3_f32 v50, v50, v41, v42
	v_max_f32_e32 v51, v52, v51
	v_max3_f32 v51, v50, v43, v51
	v_cndmask_b32_e64 v50, v50, v51, s[0:1]
	v_mov_b32_e32 v51, v50
	s_nop 1
	v_permlane32_swap_b32_e32 v50, v51
	v_max_f32_e32 v51, v51, v51
	v_max_f32_e32 v50, v50, v50
	v_max_f32_e32 v50, v50, v51
	v_sub_f32_e32 v34, v34, v50
	v_exp_f32_e32 v52, v34
	v_sub_f32_e32 v34, v35, v50
	v_sub_f32_e32 v35, v36, v50
	v_cvt_pk_f16_f32 v49, v49, v56
	v_exp_f32_e32 v56, v35
	v_sub_f32_e32 v35, v37, v50
	v_cvt_pk_f16_f32 v64, v57, v58
	v_exp_f32_e32 v57, v35
	v_sub_f32_e32 v35, v38, v50
	v_exp_f32_e32 v58, v35
	v_sub_f32_e32 v35, v39, v50
	v_cvt_pk_f16_f32 v65, v59, v60
	v_exp_f32_e32 v60, v35
	v_sub_f32_e32 v35, v40, v50
	v_cvt_pk_f16_f32 v48, v48, v55
	v_exp_f32_e32 v55, v34
	v_exp_f32_e32 v62, v35
	v_sub_f32_e32 v35, v41, v50
	v_exp_f32_e32 v63, v35
	v_sub_f32_e32 v35, v42, v50
	v_exp_f32_e32 v59, v35
	v_sub_f32_e32 v35, v43, v50
	v_add_f32_e32 v34, 0, v52
	v_exp_f32_e32 v35, v35
	v_add_f32_e32 v34, v55, v34
	v_add_f32_e32 v34, v56, v34
	v_add_f32_e32 v34, v57, v34
	v_add_f32_e32 v34, v58, v34
	v_cndmask_b32_e64 v61, v35, 0, s[14:15]
	v_sub_f32_e32 v35, v44, v50
	v_add_f32_e32 v34, v60, v34
	v_exp_f32_e32 v35, v35
	v_sub_f32_e32 v36, v45, v50
	v_cvt_pk_f16_f32 v25, v24, v25
	v_cvt_pk_f16_f32 v24, v22, v23
	v_cvt_pk_f16_f32 v23, v20, v21
	v_cvt_pk_f16_f32 v22, v18, v19
	v_add_f32_e32 v34, v62, v34
	v_exp_f32_e32 v36, v36
	v_add_f32_e32 v34, v63, v34
	v_add_f32_e32 v34, v59, v34
	v_add_f32_e32 v34, v61, v34
	v_cndmask_b32_e64 v211, v35, 0, s[14:15]
	v_add_f32_e32 v18, v211, v34
	v_cndmask_b32_e64 v250, v36, 0, s[14:15]
	v_cvt_pk_f16_f32 v51, v32, v33
	v_mfma_f32_32x32x16_f16 v[32:47], v[22:25], v[46:49], 0
	v_cvt_pk_f16_f32 v50, v30, v31
	v_cvt_pk_f16_f32 v49, v28, v29
	v_cvt_pk_f16_f32 v48, v26, v27
	v_mov_b32_e32 v67, v66
	v_add_f32_e32 v251, v250, v18
	v_mov_b32_e32 v54, v53
	v_mov_b32_e32 v252, v251
	v_mfma_f32_32x32x16_f16 v[32:47], v[48:51], v[64:67], v[32:47]
	v_permlane32_swap_b32_e32 v53, v54
	v_permlane32_swap_b32_e32 v251, v252
	s_and_saveexec_b64 s[2:3], s[4:5]
	s_cbranch_execz .LBB1_55
	v_add_f32_e32 v18, v53, v54
	v_rcp_f32_e32 v18, v18
	s_nop 5
	v_mov_b32_e32 v20, v33
	v_mov_b32_e32 v21, v34
	v_mov_b32_e32 v26, v37
	v_fma_mixlo_f16 v19, v18, v32, 0
	v_pk_mul_f32 v[20:21], v[18:19], v[20:21] op_sel_hi:[0,1]
	v_mov_b32_e32 v27, v38
	v_cvt_pk_f16_f32 v21, v20, v21
	v_pk_mul_f32 v[26:27], v[18:19], v[26:27] op_sel_hi:[0,1]
	v_fma_mixlo_f16 v28, v18, v36, 0
	v_pack_b32_f16 v20, v19, v21
	v_cvt_pk_f16_f32 v19, v26, v27
	v_fma_mixlo_f16 v27, v18, v35, 0
	v_fma_mixlo_f16 v18, v18, v39, 0
	v_pack_b32_f16 v26, v28, v19
	v_alignbit_b32 v21, v27, v21, 16
	v_alignbit_b32 v27, v18, v19, 16
	ds_write2_b64 v247, v[20:21], v[26:27] offset1:2
